# P8 next-unit prefetch: 7 row addresses as 32-bit row*5120+col offsets on an SGPR base (no v_mad_u64_u32 / 64-bit adds), on top of v98
# baseline (speedup 1.0000x reference)
.LBB0_1303:
	s_and_b64 s[54:55], exec, s[54:55]
	s_cselect_b32 s54, 15, 1
	s_cselect_b32 s20, s67, 0x100
	s_and_b32 s54, s54, s56
	s_lshl_b32 s54, s54, 7
	v_or_b32_e32 v30, s54, v1
	s_add_i32 s60, s20, -1
	s_sub_u32 s54, s58, s54
	s_subb_u32 s55, s59, 0
	s_mulk_i32 s56, 0xfb00
	s_add_i32 s57, s45, s35
	s_add_i32 s56, s57, s56
	s_ashr_i32 s57, s56, 31
	s_lshl_b64 s[56:57], s[56:57], 1
	s_add_u32 s100, s6, s56
	s_addc_u32 s101, s7, s57
	v_or_b32_e32 v31, 1, v30
	v_or_b32_e32 v32, 2, v30
	v_or_b32_e32 v33, 3, v30
	v_add_u32_e32 v34, 4, v30
	v_lshlrev_b32_e32 v246, 1, v158
	v_max_i32_e32 v247, 2, v30
	v_add_u32_e32 v247, -2, v247
	v_min_u32_e32 v247, s60, v247
	v_add_u32_e32 v247, s54, v247
	v_mad_u32_u24 v247, v247, s78, v246
	global_load_dwordx4 v[38:41], v247, s[100:101] offset:2560
	v_max_i32_e32 v247, 1, v30
	v_add_u32_e32 v247, -1, v247
	v_min_u32_e32 v247, s60, v247
	v_add_u32_e32 v247, s54, v247
	v_mad_u32_u24 v247, v247, s78, v246
	global_load_dwordx4 v[42:45], v247, s[100:101] offset:2560
	v_min_u32_e32 v247, s60, v30
	v_add_u32_e32 v247, s54, v247
	v_mad_u32_u24 v247, v247, s78, v246
	global_load_dwordx4 v[46:49], v247, s[100:101] offset:2560
	v_min_u32_e32 v247, s60, v31
	v_add_u32_e32 v247, s54, v247
	v_mad_u32_u24 v247, v247, s78, v246
	global_load_dwordx4 v[50:53], v247, s[100:101] offset:2560
	v_min_u32_e32 v247, s60, v32
	v_add_u32_e32 v247, s54, v247
	v_mad_u32_u24 v247, v247, s78, v246
	global_load_dwordx4 v[54:57], v247, s[100:101] offset:2560
	v_min_u32_e32 v247, s60, v33
	v_add_u32_e32 v247, s54, v247
	v_mad_u32_u24 v247, v247, s78, v246
	global_load_dwordx4 v[58:61], v247, s[100:101] offset:2560
	v_min_u32_e32 v247, s60, v34
	v_add_u32_e32 v247, s54, v247
	v_mad_u32_u24 v247, v247, s78, v246
	global_load_dwordx4 v[62:65], v247, s[100:101] offset:2560
	v_mov_b32_e32 v66, v30
	s_mov_b32 s99, s20
